# final RMSNorm wave reduction: first four butterfly stages use DPP adds (quad_perm, row_half_mirror, row_mirror) instead of ds_bpermute round trips
# baseline (speedup 1.0000x reference)
; __device__ __forceinline__ float f16_lo(unsigned u) { return (float)__builtin_bit_cast(h16x2, u)[0]; }
; __device__ __forceinline__ float f16_hi(unsigned u) { return (float)__builtin_bit_cast(h16x2, u)[1]; }
; #define GAS __attribute__((address_space(1)))
; __global__ void __launch_bounds__(NWAVES * 64, 2) mk_fwd(Args args) {
;     ...
;           for (; m < M; m += 2 * NGW) { f32x4 v[2][4]; float ss[2] = {0.f, 0.f};
; #pragma unroll
;               for (int r = 0; r < 2; ++r) { const GAS v2u* xr = (const GAS v2u*)(hx + (size_t)(m + r * NGW) * D) + ln;
; #pragma unroll
;                   for (int q = 0; q < 4; ++q) { const v2u hv = xr[64 * q]; v[r][q] = (f32x4){pg8::f16_lo(hv.x), pg8::f16_hi(hv.x), pg8::f16_lo(hv.y), pg8::f16_hi(hv.y)}; } }
; #pragma unroll
;               for (int r = 0; r < 2; ++r) {
; #pragma unroll
;                   for (int q = 0; q < 4; ++q) ss[r] += (v[r][q].x * v[r][q].x + v[r][q].y * v[r][q].y) + (v[r][q].z * v[r][q].z + v[r][q].w * v[r][q].w);
.LBB0_1358:
	s_ashr_i32 s61, s60, 31
	s_lshl_b64 s[2:3], s[60:61], 11
	s_add_u32 s2, s1, s2
	s_addc_u32 s3, s4, s3
	v_lshl_add_u64 v[16:17], s[2:3], 0, v[4:5]
	global_load_dwordx2 v[20:21], v[16:17], off
	global_load_dwordx2 v[22:23], v[16:17], off offset:512
	global_load_dwordx2 v[24:25], v[16:17], off offset:1024
	s_add_i32 s2, s54, s60
	global_load_dwordx2 v[26:27], v[16:17], off offset:1536
	s_ashr_i32 s3, s2, 31
	s_lshl_b64 s[8:9], s[2:3], 11
	s_add_u32 s8, s1, s8
	s_addc_u32 s9, s4, s9
	v_lshl_add_u64 v[28:29], s[8:9], 0, v[4:5]
	global_load_dwordx2 v[30:31], v[28:29], off
	global_load_dwordx2 v[32:33], v[28:29], off offset:512
	global_load_dwordx2 v[34:35], v[28:29], off offset:1024
	global_load_dwordx2 v[36:37], v[28:29], off offset:1536
	s_lshl_b64 s[8:9], s[60:61], 12
	s_lshl_b64 s[2:3], s[2:3], 12
	s_add_i32 s60, s60, s5
	s_cmpk_lt_i32 s60, 0x4000
	s_waitcnt vmcnt(0)
	v_cvt_f32_f16_e32 v28, v20
	v_cvt_f32_f16_sdwa v29, v20 dst_sel:DWORD dst_unused:UNUSED_PAD src0_sel:WORD_1
	v_cvt_f32_f16_e32 v20, v21
	v_cvt_f32_f16_sdwa v21, v21 dst_sel:DWORD dst_unused:UNUSED_PAD src0_sel:WORD_1
	v_cvt_f32_f16_e32 v40, v22
	v_cvt_f32_f16_sdwa v41, v22 dst_sel:DWORD dst_unused:UNUSED_PAD src0_sel:WORD_1
	v_cvt_f32_f16_e32 v22, v23
	v_cvt_f32_f16_sdwa v23, v23 dst_sel:DWORD dst_unused:UNUSED_PAD src0_sel:WORD_1
	v_cvt_f32_f16_e32 v42, v24
	v_cvt_f32_f16_sdwa v43, v24 dst_sel:DWORD dst_unused:UNUSED_PAD src0_sel:WORD_1
	v_cvt_f32_f16_e32 v24, v25
	v_cvt_f32_f16_sdwa v25, v25 dst_sel:DWORD dst_unused:UNUSED_PAD src0_sel:WORD_1
	v_cvt_f32_f16_e32 v44, v26
	v_cvt_f32_f16_sdwa v45, v26 dst_sel:DWORD dst_unused:UNUSED_PAD src0_sel:WORD_1
	v_cvt_f32_f16_e32 v26, v27
	v_cvt_f32_f16_sdwa v27, v27 dst_sel:DWORD dst_unused:UNUSED_PAD src0_sel:WORD_1
	v_cvt_f32_f16_e32 v46, v30
	v_cvt_f32_f16_sdwa v47, v30 dst_sel:DWORD dst_unused:UNUSED_PAD src0_sel:WORD_1
	v_cvt_f32_f16_e32 v30, v31
	v_cvt_f32_f16_sdwa v31, v31 dst_sel:DWORD dst_unused:UNUSED_PAD src0_sel:WORD_1
	v_cvt_f32_f16_e32 v48, v32
	v_cvt_f32_f16_sdwa v49, v32 dst_sel:DWORD dst_unused:UNUSED_PAD src0_sel:WORD_1
	v_cvt_f32_f16_e32 v32, v33
	v_cvt_f32_f16_sdwa v33, v33 dst_sel:DWORD dst_unused:UNUSED_PAD src0_sel:WORD_1
	v_mov_b32_e32 v56, v29
	v_mov_b32_e32 v57, v21
	v_mov_b32_e32 v60, v41
	v_mov_b32_e32 v61, v23
	v_mov_b32_e32 v54, v28
	v_mov_b32_e32 v55, v20
	v_mov_b32_e32 v58, v40
	v_mov_b32_e32 v59, v22
	v_mul_f32_e32 v62, v43, v43
	v_mul_f32_e32 v64, v25, v25
	v_pk_mul_f32 v[56:57], v[56:57], v[56:57]
	v_pk_mul_f32 v[60:61], v[60:61], v[60:61]
	v_cvt_f32_f16_e32 v50, v34
	v_cvt_f32_f16_sdwa v51, v34 dst_sel:DWORD dst_unused:UNUSED_PAD src0_sel:WORD_1
	v_cvt_f32_f16_e32 v34, v35
	v_cvt_f32_f16_sdwa v35, v35 dst_sel:DWORD dst_unused:UNUSED_PAD src0_sel:WORD_1
	v_pk_mul_f32 v[68:69], v[26:27], v[26:27]
	v_pk_fma_f32 v[62:63], v[42:43], v[42:43], v[62:63] op_sel_hi:[1,1,0]
	v_pk_fma_f32 v[64:65], v[24:25], v[24:25], v[64:65] op_sel_hi:[1,1,0]
	v_pk_fma_f32 v[54:55], v[54:55], v[54:55], v[56:57]
	v_pk_fma_f32 v[56:57], v[58:59], v[58:59], v[60:61]
	v_cvt_f32_f16_e32 v52, v36
	v_cvt_f32_f16_sdwa v53, v36 dst_sel:DWORD dst_unused:UNUSED_PAD src0_sel:WORD_1
	v_cvt_f32_f16_e32 v36, v37
	v_cvt_f32_f16_sdwa v37, v37 dst_sel:DWORD dst_unused:UNUSED_PAD src0_sel:WORD_1
	v_pk_mul_f32 v[66:67], v[44:45], v[44:45]
	v_mov_b32_e32 v63, v68
	v_mov_b32_e32 v65, v69
	v_pk_add_f32 v[54:55], v[54:55], v[54:55] op_sel:[0,1] op_sel_hi:[1,0]
	v_pk_add_f32 v[56:57], v[56:57], v[56:57] op_sel:[0,1] op_sel_hi:[1,0]
	v_pk_add_f32 v[58:59], v[62:63], v[64:65]
	v_mov_b32_e32 v55, v66
	v_mov_b32_e32 v57, v67
	v_mov_b32_e32 v62, v47
	v_mov_b32_e32 v63, v31
	v_mov_b32_e32 v66, v49
	v_mov_b32_e32 v67, v33
	v_mov_b32_e32 v60, v46
	v_mov_b32_e32 v61, v30
	v_mov_b32_e32 v64, v48
	v_mov_b32_e32 v65, v32
	v_pk_add_f32 v[54:55], v[54:55], v[56:57]
	v_pk_mul_f32 v[56:57], v[62:63], v[62:63]
	v_pk_mul_f32 v[62:63], v[66:67], v[66:67]
	v_mul_f32_e32 v68, v51, v51
	v_mul_f32_e32 v70, v35, v35
	v_pk_add_f32 v[54:55], v[54:55], v[58:59]
	v_pk_fma_f32 v[56:57], v[60:61], v[60:61], v[56:57]
	v_pk_fma_f32 v[58:59], v[64:65], v[64:65], v[62:63]
	v_pk_fma_f32 v[66:67], v[50:51], v[50:51], v[68:69] op_sel_hi:[1,1,0]
	v_pk_add_f32 v[56:57], v[56:57], v[56:57] op_sel:[0,1] op_sel_hi:[1,0]
	v_pk_add_f32 v[58:59], v[58:59], v[58:59] op_sel:[0,1] op_sel_hi:[1,0]
	v_pk_fma_f32 v[60:61], v[34:35], v[34:35], v[70:71] op_sel_hi:[1,1,0]
	v_pk_mul_f32 v[62:63], v[52:53], v[52:53]
	v_pk_mul_f32 v[64:65], v[36:37], v[36:37]
	v_mov_b32_e32 v57, v62
	v_mov_b32_e32 v59, v63
	v_mov_b32_e32 v67, v64
	v_mov_b32_e32 v61, v65
	v_pk_add_f32 v[56:57], v[56:57], v[58:59]
	v_pk_add_f32 v[58:59], v[66:67], v[60:61]
	s_waitcnt lgkmcnt(0)
; #define GAS __attribute__((address_space(1)))
; __device__ __forceinline__ float wave_sum(float v, int lane) {
; #pragma unroll
;     for (int o = 1; o < 64; o <<= 1) v += __builtin_bit_cast(float, __builtin_amdgcn_ds_bpermute((lane ^ o) << 2, __builtin_bit_cast(int, v)));
;     return v;
; __global__ void __launch_bounds__(NWAVES * 64, 2) mk_fwd(Args args) {
;     ...
;               for (int r = 0; r < 2; ++r) {
; #pragma unroll
;                   for (int q = 0; q < 4; ++q) ss[r] += (v[r][q].x * v[r][q].x + v[r][q].y * v[r][q].y) + (v[r][q].z * v[r][q].z + v[r][q].w * v[r][q].w);
;                   const float rstd = rsqrtf(wave_sum(ss[r], ln) * (1.f / D) + EPS); GAS f32x4* o = (GAS f32x4*)(ap->out + (size_t)(m + r * NGW) * D) + ln;
; #pragma unroll
;                   for (int q = 0; q < 4; ++q) o[64 * q] = v[r][q] * rstd * gr[64 * q]; } } }
	v_lshl_add_u64 v[38:39], v[88:89], 0, s[8:9]
	v_pk_add_f32 v[56:57], v[56:57], v[58:59]
	v_mov_b32_e32 v59, v54
	v_mov_b32_e32 v58, v56
	v_mov_b32_e32 v54, v57
	v_pk_add_f32 v[54:55], v[58:59], v[54:55]
	s_nop 1
	v_add_f32_dpp v54, v54, v54 quad_perm:[1,0,3,2] row_mask:0xf bank_mask:0xf
	v_add_f32_dpp v55, v55, v55 quad_perm:[1,0,3,2] row_mask:0xf bank_mask:0xf
	s_nop 1
	v_add_f32_dpp v54, v54, v54 quad_perm:[2,3,0,1] row_mask:0xf bank_mask:0xf
	v_add_f32_dpp v55, v55, v55 quad_perm:[2,3,0,1] row_mask:0xf bank_mask:0xf
	s_nop 1
	v_add_f32_dpp v54, v54, v54 row_half_mirror row_mask:0xf bank_mask:0xf
	v_add_f32_dpp v55, v55, v55 row_half_mirror row_mask:0xf bank_mask:0xf
	s_nop 1
	v_add_f32_dpp v54, v54, v54 row_mirror row_mask:0xf bank_mask:0xf
	v_add_f32_dpp v55, v55, v55 row_mirror row_mask:0xf bank_mask:0xf
	s_nop 1
	ds_bpermute_b32 v57, v13, v55
	ds_bpermute_b32 v56, v13, v54
	s_waitcnt lgkmcnt(0)
	v_pk_add_f32 v[54:55], v[54:55], v[56:57]
	ds_bpermute_b32 v57, v14, v55
	ds_bpermute_b32 v56, v14, v54
	s_waitcnt lgkmcnt(0)
	v_pk_add_f32 v[54:55], v[54:55], v[56:57]
	s_nop 0
	v_pk_fma_f32 v[54:55], v[54:55], s[0:1], v[2:3] op_sel_hi:[1,0,0]
	s_nop 0
	v_mul_f32_e32 v15, 0x4b800000, v55
	v_cmp_gt_f32_e32 vcc, s6, v55
	s_nop 1
	v_cndmask_b32_e32 v15, v55, v15, vcc
	v_rsq_f32_e32 v15, v15
	s_nop 0
	v_mul_f32_e32 v55, 0x45800000, v15
	v_cndmask_b32_e32 v56, v15, v55, vcc
	v_pk_mul_f32 v[28:29], v[56:57], v[28:29] op_sel_hi:[0,1]
	v_pk_mul_f32 v[20:21], v[56:57], v[20:21] op_sel_hi:[0,1]
	v_pk_mul_f32 v[18:19], v[20:21], v[74:75]
	v_pk_mul_f32 v[16:17], v[28:29], v[72:73]
	global_store_dwordx4 v[38:39], v[16:19], off sc1
	v_pk_mul_f32 v[20:21], v[56:57], v[22:23] op_sel_hi:[0,1]
	v_pk_mul_f32 v[22:23], v[56:57], v[40:41] op_sel_hi:[0,1]
	v_mul_f32_e32 v15, 0x4b800000, v54
	v_cmp_gt_f32_e32 vcc, s6, v54
	v_pk_mul_f32 v[90:91], v[22:23], v[76:77]
	v_pk_mul_f32 v[92:93], v[20:21], v[78:79]
	global_store_dwordx4 v[38:39], v[90:93], off offset:1024 sc1
	v_pk_mul_f32 v[20:21], v[56:57], v[24:25] op_sel_hi:[0,1]
	v_pk_mul_f32 v[22:23], v[56:57], v[42:43] op_sel_hi:[0,1]
	v_cndmask_b32_e32 v15, v54, v15, vcc
	v_rsq_f32_e32 v15, v15
	v_pk_mul_f32 v[94:95], v[22:23], v[80:81]
	v_pk_mul_f32 v[96:97], v[20:21], v[82:83]
	global_store_dwordx4 v[38:39], v[94:97], off offset:2048 sc1
	v_pk_mul_f32 v[20:21], v[56:57], v[26:27] op_sel_hi:[0,1]
	v_pk_mul_f32 v[22:23], v[56:57], v[44:45] op_sel_hi:[0,1]
	v_pk_mul_f32 v[98:99], v[22:23], v[84:85]
	v_pk_mul_f32 v[100:101], v[20:21], v[86:87]
	global_store_dwordx4 v[38:39], v[98:101], off offset:3072 sc1
	v_mul_f32_e32 v22, 0x45800000, v15
	v_cndmask_b32_e32 v22, v15, v22, vcc
	v_pk_mul_f32 v[24:25], v[22:23], v[30:31] op_sel_hi:[0,1]
	v_pk_mul_f32 v[26:27], v[22:23], v[46:47] op_sel_hi:[0,1]
	v_lshl_add_u64 v[20:21], v[88:89], 0, s[2:3]
	v_pk_mul_f32 v[102:103], v[26:27], v[72:73]
	v_pk_mul_f32 v[104:105], v[24:25], v[74:75]
	global_store_dwordx4 v[20:21], v[102:105], off sc1
	v_pk_mul_f32 v[24:25], v[22:23], v[32:33] op_sel_hi:[0,1]
	v_pk_mul_f32 v[26:27], v[22:23], v[48:49] op_sel_hi:[0,1]
	v_pk_mul_f32 v[106:107], v[26:27], v[76:77]
	v_pk_mul_f32 v[108:109], v[24:25], v[78:79]
	global_store_dwordx4 v[20:21], v[106:109], off offset:1024 sc1
	v_pk_mul_f32 v[24:25], v[22:23], v[34:35] op_sel_hi:[0,1]
	v_pk_mul_f32 v[26:27], v[22:23], v[50:51] op_sel_hi:[0,1]
	v_pk_mul_f32 v[110:111], v[26:27], v[80:81]
	v_pk_mul_f32 v[112:113], v[24:25], v[82:83]
	global_store_dwordx4 v[20:21], v[110:113], off offset:2048 sc1
	v_pk_mul_f32 v[24:25], v[22:23], v[36:37] op_sel_hi:[0,1]
	v_pk_mul_f32 v[22:23], v[22:23], v[52:53] op_sel_hi:[0,1]
	v_pk_mul_f32 v[114:115], v[22:23], v[84:85]
	v_pk_mul_f32 v[116:117], v[24:25], v[86:87]
	global_store_dwordx4 v[20:21], v[114:117], off offset:3072 sc1
	s_cbranch_scc1 .LBB0_1358
